# Prologue: the converted layer-0 FFN weights (first needed ~600 us later) are stored with the nt hint so they do not displace the W_in operands
# speedup vs baseline: 1.0103x; 1.0103x over previous
; __device__ __forceinline__ unsigned cvt_pk_bf16(float lo, float hi) { f32x2_t v = {lo, hi}; bf16x2_t b = __builtin_convertvector(v, bf16x2_t); return __builtin_bit_cast(unsigned, b); }
;     const int c = lane & 7, nn = lane >> 3;
;     const float* src0 = W + (size_t)(kb * 64 + 8 * c) * ldw;
; #pragma unroll 2
;     for (int sb = sb0; sb < sb1; ++sb) {
;         const int n = nb * 256 + sb * 32 + 4 * nn;
;         if (n < N) {
;             int r = n;
;             if (rowmode == 1) r = n < 2608 ? n : n + 208;
;             else if (rowmode == 2) r = ((n >> 7) << 8) + (n & 127);
;             else if (rowmode == 3) r = ((n >> 7) << 8) + 128 + (n & 127);
;             const float* src = src0 + n;
;             f32x4 v[8];
; #pragma unroll
;             for (int i = 0; i < 8; ++i) v[i] = *(const f32x4*)(src + (size_t)i * ldw);
;             bf16* d0 = WT + (size_t)r * K + kb * 64 + 8 * c;
; #pragma unroll
;             for (int j = 0; j < 4; ++j) { u32x4 o; o.x = cvt_pk_bf16(v[0][j], v[1][j]); o.y = cvt_pk_bf16(v[2][j], v[3][j]); o.z = cvt_pk_bf16(v[4][j], v[5][j]); o.w = cvt_pk_bf16(v[6][j], v[7][j]);
;                 *(u32x4*)(d0 + (size_t)j * K) = o; }
;         }
;     }
; }
; __global__ void __launch_bounds__(NWAVES * 64, 2) trunk_fwd(Args args) {
;     ...
;                 int r = it;
;                 if (r < C_WIN) { const int l = r / (32 * 35), q = r % (32 * 35); conv_tile(args.in[I_WIN] + (size_t)l * D * IN_W, IN_W, D, IN_W, WIN_T + (size_t)l * ZLD * D, 1, q / 35, q % 35, lane, wave, wave + 1); continue; } r -= C_WIN;
;                 if (r < C_WAB) { const int ab = r / (2 * 16 * 8), l = (r / (16 * 8)) & 1, q = r % (16 * 8); conv_tile(args.in[ab ? I_WB : I_WA] + (size_t)l * 1024 * 2048, 2048, 1024, 2048, (ab ? WB_T : WA_T) + (size_t)l * 2048 * 1024, 0, q / 8, q % 8, lane, wave, wave + 1); continue; } r -= C_WAB;
;                 if (r < C_WO) { const int l = r / (32 * 8), q = r % (32 * 8); conv_tile(args.in[I_WO] + (size_t)l * 2048 * 2048, 2048, 2048, 2048, WO_T + (size_t)l * 2048 * 2048, 0, q / 8, q % 8, lane, wave, wave + 1); continue; } r -= C_WO;
;                 if (r < C_CW1) { const int lk = r / 32, q = r % 32; conv_tile(args.in[(lk & 1) ? I_VW1 : I_KW1] + (size_t)(lk >> 1) * 2048 * 256, 256, 2048, 256, CW1_T + (size_t)lk * 256 * 2048, 0, q, 0, lane, wave, wave + 1); continue; } r -= C_CW1;
.LBB0_25:
	s_cmpk_gt_i32 s67, 0x8bf
	s_mov_b64 s[20:21], -1
	s_cbranch_scc0 .LBB0_54
	s_cmpk_gt_u32 s67, 0xabf
	s_cbranch_scc0 .LBB0_50
	s_cmpk_gt_u32 s67, 0xcbf
	s_cbranch_scc0 .LBB0_46
	s_cmpk_gt_u32 s67, 0xd3f
	s_cbranch_scc0 .LBB0_42
	s_cmpk_gt_u32 s67, 0xd4f
	s_cbranch_scc0 .LBB0_38
	s_cmpk_gt_u32 s67, 0x12cf
	s_cbranch_scc0 .LBB0_34
	s_and_b32 s2, s31, 0x700
	s_add_i32 s20, s30, s2
	s_cmpk_gt_u32 s20, 0x7ff
	s_cbranch_scc1 .LBB0_33
	s_and_b32 s2, s66, 0x7fffffc0
	s_add_i32 s18, s2, 0xffff6980
	v_or_b32_e32 v4, s18, v2
	v_lshlrev_b64 v[18:19], 13, v[4:5]
	s_waitcnt lgkmcnt(0)
	v_lshl_add_u64 v[18:19], s[4:5], 0, v[18:19]
	v_or_b32_e32 v4, s20, v3
	v_lshl_add_u64 v[42:43], v[4:5], 2, v[18:19]
	v_add_co_u32_e32 v22, vcc, 0x2000, v42
	v_lshl_add_u64 v[50:51], s[18:19], 1, v[6:7]
	s_nop 0
	v_addc_co_u32_e32 v23, vcc, 0, v43, vcc
	v_add_co_u32_e32 v26, vcc, 0x4000, v42
	global_load_dwordx4 v[18:21], v[42:43], off nt
	s_nop 0
	global_load_dwordx4 v[22:25], v[22:23], off nt
	v_addc_co_u32_e32 v27, vcc, 0, v43, vcc
	v_add_co_u32_e32 v30, vcc, 0x6000, v42
	v_mad_u64_u32 v[58:59], s[20:21], v4, s44, v[50:51]
	s_nop 0
	v_addc_co_u32_e32 v31, vcc, 0, v43, vcc
	v_add_co_u32_e32 v34, vcc, 0x8000, v42
	global_load_dwordx4 v[26:29], v[26:27], off nt
	s_nop 0
	global_load_dwordx4 v[30:33], v[30:31], off nt
	v_addc_co_u32_e32 v35, vcc, 0, v43, vcc
	v_add_co_u32_e32 v38, vcc, 0xa000, v42
	s_waitcnt vmcnt(2)
	v_cvt_pk_bf16_f32 v18, v18, v22
	v_addc_co_u32_e32 v39, vcc, 0, v43, vcc
	v_add_co_u32_e32 v44, vcc, 0xc000, v42
	global_load_dwordx4 v[34:37], v[34:35], off nt
	s_nop 0
	global_load_dwordx4 v[38:41], v[38:39], off nt
	v_addc_co_u32_e32 v45, vcc, 0, v43, vcc
	v_add_co_u32_e32 v46, vcc, 0xe000, v42
	v_cvt_pk_bf16_f32 v22, v19, v23
	s_nop 0
	v_addc_co_u32_e32 v47, vcc, 0, v43, vcc
	global_load_dwordx4 v[42:45], v[44:45], off nt
	s_nop 0
	global_load_dwordx4 v[46:49], v[46:47], off nt
	v_add_co_u32_e32 v60, vcc, s37, v58
	v_cvt_pk_bf16_f32 v50, v20, v24
	s_nop 0
	v_addc_co_u32_e32 v61, vcc, 0, v59, vcc
	v_add_co_u32_e32 v62, vcc, s45, v58
	v_cvt_pk_bf16_f32 v54, v21, v25
	s_nop 0
	v_addc_co_u32_e32 v63, vcc, 0, v59, vcc
	v_add_co_u32_e32 v64, vcc, 0x8000, v58
	s_waitcnt vmcnt(4)
	v_cvt_pk_bf16_f32 v19, v26, v30
	v_addc_co_u32_e32 v65, vcc, 0, v59, vcc
	v_cvt_pk_bf16_f32 v23, v27, v31
	v_cvt_pk_bf16_f32 v51, v28, v32
	v_cvt_pk_bf16_f32 v55, v29, v33
	s_waitcnt vmcnt(2)
	v_cvt_pk_bf16_f32 v20, v34, v38
	v_cvt_pk_bf16_f32 v24, v35, v39
	v_cvt_pk_bf16_f32 v52, v36, v40
	v_cvt_pk_bf16_f32 v56, v37, v41
	s_waitcnt vmcnt(0)
	v_cvt_pk_bf16_f32 v21, v42, v46
	v_cvt_pk_bf16_f32 v25, v43, v47
	v_cvt_pk_bf16_f32 v53, v44, v48
	v_cvt_pk_bf16_f32 v57, v45, v49
	global_store_dwordx4 v[58:59], v[18:21], off nt
	global_store_dwordx4 v[60:61], v[22:25], off offset:3072 nt
	global_store_dwordx4 v[62:63], v[50:53], off offset:2048 nt
	global_store_dwordx4 v[64:65], v[54:57], off offset:1024 nt

; __device__ __forceinline__ unsigned cvt_pk_bf16(float lo, float hi) { f32x2_t v = {lo, hi}; bf16x2_t b = __builtin_convertvector(v, bf16x2_t); return __builtin_bit_cast(unsigned, b); }
;     const int c = lane & 7, nn = lane >> 3;
;     const float* src0 = W + (size_t)(kb * 64 + 8 * c) * ldw;
; #pragma unroll 2
;     for (int sb = sb0; sb < sb1; ++sb) {
;         const int n = nb * 256 + sb * 32 + 4 * nn;
;         if (n < N) {
;             int r = n;
;             if (rowmode == 1) r = n < 2608 ? n : n + 208;
;             else if (rowmode == 2) r = ((n >> 7) << 8) + (n & 127);
;             else if (rowmode == 3) r = ((n >> 7) << 8) + 128 + (n & 127);
;             const float* src = src0 + n;
;             f32x4 v[8];
; #pragma unroll
;             for (int i = 0; i < 8; ++i) v[i] = *(const f32x4*)(src + (size_t)i * ldw);
;             bf16* d0 = WT + (size_t)r * K + kb * 64 + 8 * c;
; #pragma unroll
;             for (int j = 0; j < 4; ++j) { u32x4 o; o.x = cvt_pk_bf16(v[0][j], v[1][j]); o.y = cvt_pk_bf16(v[2][j], v[3][j]); o.z = cvt_pk_bf16(v[4][j], v[5][j]); o.w = cvt_pk_bf16(v[6][j], v[7][j]);
;                 *(u32x4*)(d0 + (size_t)j * K) = o; }
;         }
;     }
; }
; __global__ void __launch_bounds__(NWAVES * 64, 2) trunk_fwd(Args args) {
;     ...
;                 if (r < C_F13) { const int w3 = r / (32 * 22), q = r % (32 * 22); conv_tile(args.in[w3 ? I_F3 : I_F1], FFD, D, FFD, FUP_T, 2 + w3, q / 22, q % 22, lane, wave, wave + 1); continue; } r -= C_F13;
.LBB0_34:
	s_andn2_b64 vcc, exec, s[20:21]
	s_cbranch_vccnz .LBB0_37
	s_add_i32 s68, s67, 0xfffff2b0
	s_add_i32 s2, s67, 0xffffeff0
	s_cmpk_lt_u32 s68, 0x2c0
	s_cselect_b64 s[20:21], -1, 0
	s_and_b64 s[70:71], s[20:21], exec
	s_cselect_b32 s2, s68, s2
	s_mul_hi_u32 s18, s2, 0xba2e8ba3
	s_lshr_b32 s70, s18, 4
	s_mul_i32 s18, s70, 22
	s_sub_i32 s2, s2, s18
	s_lshl_b32 s2, s2, 8
	s_add_i32 s69, s30, s2
	s_cmpk_gt_u32 s69, 0x15ff
	s_cbranch_scc1 .LBB0_37
	s_lshl_b32 s18, s70, 7
	s_and_b64 s[20:21], s[20:21], exec
	s_cselect_b32 s2, s46, 0x90
	s_add_u32 s20, s0, s2
	s_addc_u32 s21, s1, 0
	s_load_dwordx2 s[20:21], s[20:21], 0x0
	v_lshl_or_b32 v17, s70, 6, v2
	v_or_b32_e32 v4, s69, v3
	s_cmpk_gt_u32 s68, 0x2bf
	v_lshl_add_u64 v[50:51], v[8:9], 0, s[18:19]
	s_waitcnt lgkmcnt(0)
	v_mov_b64_e32 v[18:19], s[20:21]
	v_mad_u64_u32 v[18:19], s[20:21], v17, s47, v[18:19]
	v_lshl_add_u64 v[42:43], v[4:5], 2, v[18:19]
	v_add_co_u32_e32 v22, vcc, s45, v42
	v_bitop3_b32 v4, s69, v16, v3 bitop3:0xc8
	s_nop 0
	v_addc_co_u32_e32 v23, vcc, 0, v43, vcc
	v_add_co_u32_e32 v26, vcc, s48, v42
	global_load_dwordx4 v[18:21], v[42:43], off nt
	s_nop 0
	global_load_dwordx4 v[22:25], v[22:23], off offset:2048 nt
	v_addc_co_u32_e32 v27, vcc, 0, v43, vcc
	v_add_co_u32_e32 v30, vcc, s49, v42
	s_waitcnt vmcnt(0)
	v_cvt_pk_bf16_f32 v54, v19, v23
	v_addc_co_u32_e32 v31, vcc, 0, v43, vcc
	v_add_co_u32_e32 v34, vcc, s51, v42
	global_load_dwordx4 v[26:29], v[26:27], off nt
	s_nop 0
	global_load_dwordx4 v[30:33], v[30:31], off offset:2048 nt
	v_addc_co_u32_e32 v35, vcc, 0, v43, vcc
	v_add_co_u32_e32 v38, vcc, s52, v42
	v_cvt_pk_bf16_f32 v58, v20, v24
	s_nop 0
	v_addc_co_u32_e32 v39, vcc, 0, v43, vcc
	v_add_co_u32_e32 v44, vcc, s53, v42
	global_load_dwordx4 v[34:37], v[34:35], off nt
	s_nop 0
	global_load_dwordx4 v[38:41], v[38:39], off offset:2048 nt
	v_addc_co_u32_e32 v45, vcc, 0, v43, vcc
	v_add_co_u32_e32 v46, vcc, s54, v42
	s_waitcnt vmcnt(2)
	v_cvt_pk_bf16_f32 v55, v27, v31
	v_addc_co_u32_e32 v47, vcc, 0, v43, vcc
	global_load_dwordx4 v[42:45], v[44:45], off nt
	s_nop 0
	global_load_dwordx4 v[46:49], v[46:47], off offset:2048 nt
	s_cselect_b64 vcc, -1, 0
	s_lshl_b32 s2, s69, 1
	s_and_b32 s2, s2, 0x3f00
	v_or_b32_e32 v4, s2, v4
	v_lshlrev_b32_e32 v4, 12, v4
	v_or_b32_e32 v17, 0x80000, v4
	v_cndmask_b32_e32 v4, v4, v17, vcc
	v_lshl_add_u64 v[62:63], v[50:51], 0, v[4:5]
	v_add_co_u32_e32 v64, vcc, s37, v62
	v_cvt_pk_bf16_f32 v50, v18, v22
	s_nop 0
	v_addc_co_u32_e32 v65, vcc, 0, v63, vcc
	v_add_co_u32_e32 v66, vcc, 0x3000, v62
	v_cvt_pk_bf16_f32 v51, v26, v30
	s_waitcnt vmcnt(2)
	v_cvt_pk_bf16_f32 v52, v34, v38
	v_addc_co_u32_e32 v67, vcc, 0, v63, vcc
	v_cvt_pk_bf16_f32 v56, v35, v39
	v_cvt_pk_bf16_f32 v59, v28, v32
	v_cvt_pk_bf16_f32 v60, v36, v40
	v_cvt_pk_bf16_f32 v18, v21, v25
	v_cvt_pk_bf16_f32 v19, v29, v33
	v_cvt_pk_bf16_f32 v20, v37, v41
	s_waitcnt vmcnt(0)
	v_cvt_pk_bf16_f32 v53, v42, v46
	v_cvt_pk_bf16_f32 v57, v43, v47
	v_cvt_pk_bf16_f32 v61, v44, v48
	v_cvt_pk_bf16_f32 v21, v45, v49
	global_store_dwordx4 v[62:63], v[50:53], off nt
	global_store_dwordx4 v[64:65], v[54:57], off offset:-4096 nt
	global_store_dwordx4 v[64:65], v[58:61], off nt
	global_store_dwordx4 v[66:67], v[18:21], off nt
